# quantizer loops (all four instances): per-column absmax cross-lane reduction via DPP row_ror:8 + v_permlane16/32_swap instead of 12 ds_bpermute round trips per item; on top of v74
# baseline (speedup 1.0000x reference)
; #define LAS __attribute__((address_space(3)))
;     ...
; #pragma unroll
;         for (int g = 0; g < 8; ++g)
; #pragma unroll
;             for (int r = 0; r < 4; ++r) { mx[0] = fmaxf(mx[0], fabsf(v[g][r][0])); mx[1] = fmaxf(mx[1], fabsf(v[g][r][1])); mx[2] = fmaxf(mx[2], fabsf(v[g][r][2])); mx[3] = fmaxf(mx[3], fabsf(v[g][r][3])); }
; #pragma unroll
;         for (int c = 0; c < 4; ++c) { float m = mx[c]; m = fmaxf(m, __shfl_xor(m, 8)); m = fmaxf(m, __shfl_xor(m, 16)); m = fmaxf(m, __shfl_xor(m, 32)); mx[c] = m; }
;         if (tid == 0) MISC[2] = nxt;
;         if (kr == 0) *(LAS f32x4*)(smax + wave * 32 + 4 * n4) = mx;
.LBB0_72:
	s_or_b64 exec, exec, s[6:7]
	s_waitcnt vmcnt(10)
	v_max3_f32 v130, |v2|, 0, |v6|
	s_waitcnt vmcnt(8)
	v_max3_f32 v130, v130, |v10|, |v14|
	s_waitcnt vmcnt(26)
	v_max3_f32 v130, v130, |v18|, |v22|
	s_waitcnt vmcnt(24)
	v_max3_f32 v130, v130, |v26|, |v30|
	s_waitcnt vmcnt(22)
	v_max3_f32 v130, v130, |v34|, |v38|
	s_waitcnt vmcnt(20)
	v_max3_f32 v130, v130, |v42|, |v46|
	v_max3_f32 v131, |v3|, 0, |v7|
	s_waitcnt vmcnt(18)
	v_max3_f32 v130, v130, |v50|, |v54|
	v_max3_f32 v132, |v4|, 0, |v8|
	v_max3_f32 v131, v131, |v11|, |v15|
	s_waitcnt vmcnt(16)
	v_max3_f32 v130, v130, |v58|, |v62|
	v_max3_f32 v132, v132, |v12|, |v16|
	v_max3_f32 v131, v131, |v19|, |v23|
	s_waitcnt vmcnt(14)
	v_max3_f32 v130, v130, |v66|, |v70|
	v_max3_f32 v132, v132, |v20|, |v24|
	v_max3_f32 v131, v131, |v27|, |v31|
	s_waitcnt vmcnt(12)
	v_max3_f32 v130, v130, |v74|, |v78|
	v_max3_f32 v132, v132, |v28|, |v32|
	v_max3_f32 v131, v131, |v35|, |v39|
	s_waitcnt vmcnt(10)
	v_max3_f32 v130, v130, |v82|, |v86|
	v_max3_f32 v132, v132, |v36|, |v40|
	v_max3_f32 v131, v131, |v43|, |v47|
	s_waitcnt vmcnt(8)
	v_max3_f32 v130, v130, |v90|, |v94|
	v_max3_f32 v132, v132, |v44|, |v48|
	v_max3_f32 v131, v131, |v51|, |v55|
	s_waitcnt vmcnt(6)
	v_max3_f32 v130, v130, |v98|, |v102|
	v_max3_f32 v133, |v5|, 0, |v9|
	v_max3_f32 v132, v132, |v52|, |v56|
	v_max3_f32 v131, v131, |v59|, |v63|
	s_waitcnt vmcnt(4)
	v_max3_f32 v130, v130, |v106|, |v110|
	v_max3_f32 v133, v133, |v13|, |v17|
	v_max3_f32 v132, v132, |v60|, |v64|
	v_max3_f32 v131, v131, |v67|, |v71|
	s_waitcnt vmcnt(2)
	v_max3_f32 v130, v130, |v114|, |v118|
	v_max3_f32 v133, v133, |v21|, |v25|
	v_max3_f32 v132, v132, |v68|, |v72|
	v_max3_f32 v131, v131, |v75|, |v79|
	s_waitcnt vmcnt(0)
	v_max3_f32 v130, v130, |v122|, |v126|
	v_max3_f32 v133, v133, |v29|, |v33|
	v_max3_f32 v132, v132, |v76|, |v80|
	v_max3_f32 v131, v131, |v83|, |v87|
	v_max3_f32 v133, v133, |v37|, |v41|
	v_max3_f32 v132, v132, |v84|, |v88|
	v_max3_f32 v131, v131, |v91|, |v95|
	v_max3_f32 v133, v133, |v45|, |v49|
	v_max3_f32 v132, v132, |v92|, |v96|
	v_max3_f32 v131, v131, |v99|, |v103|
	v_max3_f32 v133, v133, |v53|, |v57|
	v_max3_f32 v132, v132, |v100|, |v104|
	v_max3_f32 v131, v131, |v107|, |v111|
	v_max3_f32 v133, v133, |v61|, |v65|
	v_max3_f32 v132, v132, |v108|, |v112|
	v_max3_f32 v131, v131, |v115|, |v119|
	v_max3_f32 v133, v133, |v69|, |v73|
	v_max3_f32 v132, v132, |v116|, |v120|
	v_max3_f32 v131, v131, |v123|, |v127|
	v_max3_f32 v133, v133, |v77|, |v81|
	v_max3_f32 v135, v132, |v124|, |v128|
	v_max3_f32 v133, v133, |v85|, |v89|
	v_max3_f32 v133, v133, |v93|, |v97|
	v_max3_f32 v133, v133, |v101|, |v105|
	v_max3_f32 v133, v133, |v109|, |v113|
	v_max3_f32 v133, v133, |v117|, |v121|
	v_max3_f32 v133, v133, |v125|, |v129|
	v_mov_b32_e32 v132, v135
	s_nop 1
	v_max_f32_dpp v130, v130, v130 row_ror:8 row_mask:0xf bank_mask:0xf
	v_max_f32_dpp v131, v131, v131 row_ror:8 row_mask:0xf bank_mask:0xf
	v_max_f32_dpp v132, v132, v132 row_ror:8 row_mask:0xf bank_mask:0xf
	v_max_f32_dpp v133, v133, v133 row_ror:8 row_mask:0xf bank_mask:0xf
	v_mov_b32_e32 v134, v130
	v_mov_b32_e32 v136, v131
	v_mov_b32_e32 v137, v132
	v_mov_b32_e32 v138, v133
	s_nop 1
	v_permlane16_swap_b32 v130, v134
	v_permlane16_swap_b32 v131, v136
	v_permlane16_swap_b32 v132, v137
	v_permlane16_swap_b32 v133, v138
	v_max_f32_e32 v130, v130, v134
	v_max_f32_e32 v131, v131, v136
	v_max_f32_e32 v132, v132, v137
	v_max_f32_e32 v133, v133, v138
	v_mov_b32_e32 v134, v130
	v_mov_b32_e32 v136, v131
	v_mov_b32_e32 v137, v132
	v_mov_b32_e32 v138, v133
	s_nop 1
	v_permlane32_swap_b32 v130, v134
	v_permlane32_swap_b32 v131, v136
	v_permlane32_swap_b32 v132, v137
	v_permlane32_swap_b32 v133, v138
	v_max_f32_e32 v130, v130, v134
	v_max_f32_e32 v131, v131, v136
	v_max_f32_e32 v132, v132, v137
	v_max_f32_e32 v133, v133, v138
	s_and_saveexec_b64 s[6:7], s[40:41]
	v_mov_b32_e32 v138, s58
	ds_write_b32 v138, v1
	s_or_b64 exec, exec, s[6:7]
	s_and_saveexec_b64 s[6:7], s[4:5]
	s_cbranch_execz .LBB0_76
	v_add_u32_e32 v1, s3, v173
	ds_write_b128 v1, v[130:133]

; #define LAS __attribute__((address_space(3)))
; #define Q_GRAB() (((stop != nullptr && xb_ld(stop) >= thr) || (quota > 0 && qleft-- <= 0)) ? (unsigned)hi : (unsigned)lo + atomicAdd(cnt, 1u))
;     ...
;         unsigned nxt = 0u; if (tid == 0) nxt = Q_GRAB();
;         signed char* Qc = Qp; float* csc = csp; const bool f8c = f8; const float qmax = f8c ? 448.0f : 127.0f, qinv = f8c ? (1.0f / 448.0f) : (1.0f / 127.0f);
;         f32x4 mx = {0.f, 0.f, 0.f, 0.f};
; #pragma unroll
;         for (int g = 0; g < 8; ++g)
; #pragma unroll
;             for (int r = 0; r < 4; ++r) { mx[0] = fmaxf(mx[0], fabsf(v[g][r][0])); mx[1] = fmaxf(mx[1], fabsf(v[g][r][1])); mx[2] = fmaxf(mx[2], fabsf(v[g][r][2])); mx[3] = fmaxf(mx[3], fabsf(v[g][r][3])); }
; #pragma unroll
;         for (int c = 0; c < 4; ++c) { float m = mx[c]; m = fmaxf(m, __shfl_xor(m, 8)); m = fmaxf(m, __shfl_xor(m, 16)); m = fmaxf(m, __shfl_xor(m, 32)); mx[c] = m; }
;         if (tid == 0) MISC[2] = nxt;
;         if (kr == 0) *(LAS f32x4*)(smax + wave * 32 + 4 * n4) = mx;
.LBB0_334:
	s_waitcnt vmcnt(10)
	v_max3_f32 v130, |v2|, 0, |v6|
	s_waitcnt vmcnt(8)
	v_max3_f32 v130, v130, |v10|, |v14|
	v_max3_f32 v130, v130, |v18|, |v22|
	v_max3_f32 v130, v130, |v26|, |v30|
	v_max3_f32 v130, v130, |v34|, |v38|
	v_max3_f32 v130, v130, |v42|, |v46|
	v_max3_f32 v131, |v3|, 0, |v7|
	v_max3_f32 v130, v130, |v50|, |v54|
	v_max3_f32 v132, |v4|, 0, |v8|
	v_max3_f32 v131, v131, |v11|, |v15|
	v_max3_f32 v130, v130, |v58|, |v62|
	v_max3_f32 v132, v132, |v12|, |v16|
	v_max3_f32 v131, v131, |v19|, |v23|
	v_max3_f32 v130, v130, |v66|, |v70|
	v_max3_f32 v132, v132, |v20|, |v24|
	v_max3_f32 v131, v131, |v27|, |v31|
	v_max3_f32 v130, v130, |v74|, |v78|
	v_max3_f32 v132, v132, |v28|, |v32|
	v_max3_f32 v131, v131, |v35|, |v39|
	v_max3_f32 v130, v130, |v82|, |v86|
	v_max3_f32 v132, v132, |v36|, |v40|
	v_max3_f32 v131, v131, |v43|, |v47|
	v_max3_f32 v130, v130, |v90|, |v94|
	v_max3_f32 v132, v132, |v44|, |v48|
	v_max3_f32 v131, v131, |v51|, |v55|
	s_waitcnt vmcnt(6)
	v_max3_f32 v130, v130, |v98|, |v102|
	v_max3_f32 v133, |v5|, 0, |v9|
	v_max3_f32 v132, v132, |v52|, |v56|
	v_max3_f32 v131, v131, |v59|, |v63|
	s_waitcnt vmcnt(4)
	v_max3_f32 v130, v130, |v106|, |v110|
	v_max3_f32 v133, v133, |v13|, |v17|
	v_max3_f32 v132, v132, |v60|, |v64|
	v_max3_f32 v131, v131, |v67|, |v71|
	s_waitcnt vmcnt(2)
	v_max3_f32 v130, v130, |v114|, |v118|
	v_max3_f32 v133, v133, |v21|, |v25|
	v_max3_f32 v132, v132, |v68|, |v72|
	v_max3_f32 v131, v131, |v75|, |v79|
	s_waitcnt vmcnt(0)
	v_max3_f32 v130, v130, |v122|, |v126|
	v_max3_f32 v133, v133, |v29|, |v33|
	v_max3_f32 v132, v132, |v76|, |v80|
	v_max3_f32 v131, v131, |v83|, |v87|
	v_max3_f32 v133, v133, |v37|, |v41|
	v_max3_f32 v132, v132, |v84|, |v88|
	v_max3_f32 v131, v131, |v91|, |v95|
	v_max3_f32 v133, v133, |v45|, |v49|
	v_max3_f32 v132, v132, |v92|, |v96|
	v_max3_f32 v131, v131, |v99|, |v103|
	v_max3_f32 v133, v133, |v53|, |v57|
	v_max3_f32 v132, v132, |v100|, |v104|
	v_max3_f32 v131, v131, |v107|, |v111|
	v_max3_f32 v133, v133, |v61|, |v65|
	v_max3_f32 v132, v132, |v108|, |v112|
	v_max3_f32 v131, v131, |v115|, |v119|
	v_max3_f32 v133, v133, |v69|, |v73|
	v_max3_f32 v132, v132, |v116|, |v120|
	v_max3_f32 v131, v131, |v123|, |v127|
	v_max3_f32 v133, v133, |v77|, |v81|
	v_max3_f32 v135, v132, |v124|, |v128|
	v_max3_f32 v133, v133, |v85|, |v89|
	v_max3_f32 v133, v133, |v93|, |v97|
	v_max3_f32 v133, v133, |v101|, |v105|
	v_max3_f32 v133, v133, |v109|, |v113|
	v_max3_f32 v133, v133, |v117|, |v121|
	v_max3_f32 v133, v133, |v125|, |v129|
	v_mov_b32_e32 v132, v135
	s_nop 1
	v_max_f32_dpp v130, v130, v130 row_ror:8 row_mask:0xf bank_mask:0xf
	v_max_f32_dpp v131, v131, v131 row_ror:8 row_mask:0xf bank_mask:0xf
	v_max_f32_dpp v132, v132, v132 row_ror:8 row_mask:0xf bank_mask:0xf
	v_max_f32_dpp v133, v133, v133 row_ror:8 row_mask:0xf bank_mask:0xf
	v_mov_b32_e32 v134, v130
	v_mov_b32_e32 v136, v131
	v_mov_b32_e32 v137, v132
	v_mov_b32_e32 v138, v133
	s_nop 1
	v_permlane16_swap_b32 v130, v134
	v_permlane16_swap_b32 v131, v136
	v_permlane16_swap_b32 v132, v137
	v_permlane16_swap_b32 v133, v138
	v_max_f32_e32 v130, v130, v134
	v_max_f32_e32 v131, v131, v136
	v_max_f32_e32 v132, v132, v137
	v_max_f32_e32 v133, v133, v138
	v_mov_b32_e32 v134, v130
	v_mov_b32_e32 v136, v131
	v_mov_b32_e32 v137, v132
	v_mov_b32_e32 v138, v133
	s_nop 1
	v_permlane32_swap_b32 v130, v134
	v_permlane32_swap_b32 v131, v136
	v_permlane32_swap_b32 v132, v137
	v_permlane32_swap_b32 v133, v138
	v_max_f32_e32 v130, v130, v134
	v_max_f32_e32 v131, v131, v136
	v_max_f32_e32 v132, v132, v137
	v_max_f32_e32 v133, v133, v138
	s_and_saveexec_b64 s[6:7], s[40:41]
	v_add_u32_e32 v1, 0x1c8, v199
	v_cmp_lt_u32_e32 vcc, 23, v201
	s_mov_b64 s[12:13], vcc
	v_cmp_le_u32_e32 vcc, 0x19c8, v1
	s_or_b64 s[12:13], s[12:13], vcc
	v_mov_b32_e32 v199, 0x1800
	s_andn2_b64 exec, exec, s[12:13]
	v_mov_b32_e32 v203, 1
	global_atomic_add v199, v171, v203, s[20:21] sc0
	s_and_b64 exec, s[6:7], s[40:41]
	global_load_dword v201, v171, s[22:23] sc1
	v_mov_b32_e32 v138, s75
	ds_write_b32 v138, v1
	s_or_b64 exec, exec, s[6:7]
	s_and_saveexec_b64 s[6:7], s[4:5]
	s_cbranch_execz .LBB0_343
	v_add_u32_e32 v1, s44, v169
	ds_write_b128 v1, v[130:133]

; #define LAS __attribute__((address_space(3)))
;     ...
; #pragma unroll
;         for (int g = 0; g < 8; ++g)
; #pragma unroll
;             for (int r = 0; r < 4; ++r) { mx[0] = fmaxf(mx[0], fabsf(v[g][r][0])); mx[1] = fmaxf(mx[1], fabsf(v[g][r][1])); mx[2] = fmaxf(mx[2], fabsf(v[g][r][2])); mx[3] = fmaxf(mx[3], fabsf(v[g][r][3])); }
; #pragma unroll
;         for (int c = 0; c < 4; ++c) { float m = mx[c]; m = fmaxf(m, __shfl_xor(m, 8)); m = fmaxf(m, __shfl_xor(m, 16)); m = fmaxf(m, __shfl_xor(m, 32)); mx[c] = m; }
;         if (tid == 0) MISC[2] = nxt;
;         if (kr == 0) *(LAS f32x4*)(smax + wave * 32 + 4 * n4) = mx;
.LBB0_1754:
	s_or_b64 exec, exec, s[6:7]
	s_waitcnt vmcnt(10)
	v_max3_f32 v130, |v2|, 0, |v6|
	s_waitcnt vmcnt(8)
	v_max3_f32 v130, v130, |v10|, |v14|
	s_waitcnt vmcnt(26)
	v_max3_f32 v130, v130, |v18|, |v22|
	s_waitcnt vmcnt(24)
	v_max3_f32 v130, v130, |v26|, |v30|
	s_waitcnt vmcnt(22)
	v_max3_f32 v130, v130, |v34|, |v38|
	s_waitcnt vmcnt(20)
	v_max3_f32 v130, v130, |v42|, |v46|
	v_max3_f32 v131, |v3|, 0, |v7|
	s_waitcnt vmcnt(18)
	v_max3_f32 v130, v130, |v50|, |v54|
	v_max3_f32 v132, |v4|, 0, |v8|
	v_max3_f32 v131, v131, |v11|, |v15|
	s_waitcnt vmcnt(16)
	v_max3_f32 v130, v130, |v58|, |v62|
	v_max3_f32 v132, v132, |v12|, |v16|
	v_max3_f32 v131, v131, |v19|, |v23|
	s_waitcnt vmcnt(14)
	v_max3_f32 v130, v130, |v66|, |v70|
	v_max3_f32 v132, v132, |v20|, |v24|
	v_max3_f32 v131, v131, |v27|, |v31|
	s_waitcnt vmcnt(12)
	v_max3_f32 v130, v130, |v74|, |v78|
	v_max3_f32 v132, v132, |v28|, |v32|
	v_max3_f32 v131, v131, |v35|, |v39|
	s_waitcnt vmcnt(10)
	v_max3_f32 v130, v130, |v82|, |v86|
	v_max3_f32 v132, v132, |v36|, |v40|
	v_max3_f32 v131, v131, |v43|, |v47|
	s_waitcnt vmcnt(8)
	v_max3_f32 v130, v130, |v90|, |v94|
	v_max3_f32 v132, v132, |v44|, |v48|
	v_max3_f32 v131, v131, |v51|, |v55|
	s_waitcnt vmcnt(6)
	v_max3_f32 v130, v130, |v98|, |v102|
	v_max3_f32 v133, |v5|, 0, |v9|
	v_max3_f32 v132, v132, |v52|, |v56|
	v_max3_f32 v131, v131, |v59|, |v63|
	s_waitcnt vmcnt(4)
	v_max3_f32 v130, v130, |v106|, |v110|
	v_max3_f32 v133, v133, |v13|, |v17|
	v_max3_f32 v132, v132, |v60|, |v64|
	v_max3_f32 v131, v131, |v67|, |v71|
	s_waitcnt vmcnt(2)
	v_max3_f32 v130, v130, |v114|, |v118|
	v_max3_f32 v133, v133, |v21|, |v25|
	v_max3_f32 v132, v132, |v68|, |v72|
	v_max3_f32 v131, v131, |v75|, |v79|
	s_waitcnt vmcnt(0)
	v_max3_f32 v130, v130, |v122|, |v126|
	v_max3_f32 v133, v133, |v29|, |v33|
	v_max3_f32 v132, v132, |v76|, |v80|
	v_max3_f32 v131, v131, |v83|, |v87|
	v_max3_f32 v133, v133, |v37|, |v41|
	v_max3_f32 v132, v132, |v84|, |v88|
	v_max3_f32 v131, v131, |v91|, |v95|
	v_max3_f32 v133, v133, |v45|, |v49|
	v_max3_f32 v132, v132, |v92|, |v96|
	v_max3_f32 v131, v131, |v99|, |v103|
	v_max3_f32 v133, v133, |v53|, |v57|
	v_max3_f32 v132, v132, |v100|, |v104|
	v_max3_f32 v131, v131, |v107|, |v111|
	v_max3_f32 v133, v133, |v61|, |v65|
	v_max3_f32 v132, v132, |v108|, |v112|
	v_max3_f32 v131, v131, |v115|, |v119|
	v_max3_f32 v133, v133, |v69|, |v73|
	v_max3_f32 v132, v132, |v116|, |v120|
	v_max3_f32 v131, v131, |v123|, |v127|
	v_max3_f32 v133, v133, |v77|, |v81|
	v_max3_f32 v135, v132, |v124|, |v128|
	v_max3_f32 v133, v133, |v85|, |v89|
	v_max3_f32 v133, v133, |v93|, |v97|
	v_max3_f32 v133, v133, |v101|, |v105|
	v_max3_f32 v133, v133, |v109|, |v113|
	v_max3_f32 v133, v133, |v117|, |v121|
	v_max3_f32 v133, v133, |v125|, |v129|
	v_mov_b32_e32 v132, v135
	s_nop 1
	v_max_f32_dpp v130, v130, v130 row_ror:8 row_mask:0xf bank_mask:0xf
	v_max_f32_dpp v131, v131, v131 row_ror:8 row_mask:0xf bank_mask:0xf
	v_max_f32_dpp v132, v132, v132 row_ror:8 row_mask:0xf bank_mask:0xf
	v_max_f32_dpp v133, v133, v133 row_ror:8 row_mask:0xf bank_mask:0xf
	v_mov_b32_e32 v134, v130
	v_mov_b32_e32 v136, v131
	v_mov_b32_e32 v137, v132
	v_mov_b32_e32 v138, v133
	s_nop 1
	v_permlane16_swap_b32 v130, v134
	v_permlane16_swap_b32 v131, v136
	v_permlane16_swap_b32 v132, v137
	v_permlane16_swap_b32 v133, v138
	v_max_f32_e32 v130, v130, v134
	v_max_f32_e32 v131, v131, v136
	v_max_f32_e32 v132, v132, v137
	v_max_f32_e32 v133, v133, v138
	v_mov_b32_e32 v134, v130
	v_mov_b32_e32 v136, v131
	v_mov_b32_e32 v137, v132
	v_mov_b32_e32 v138, v133
	s_nop 1
	v_permlane32_swap_b32 v130, v134
	v_permlane32_swap_b32 v131, v136
	v_permlane32_swap_b32 v132, v137
	v_permlane32_swap_b32 v133, v138
	v_max_f32_e32 v130, v130, v134
	v_max_f32_e32 v131, v131, v136
	v_max_f32_e32 v132, v132, v137
	v_max_f32_e32 v133, v133, v138
	s_and_saveexec_b64 s[6:7], s[40:41]
	v_mov_b32_e32 v138, s3
	ds_write_b32 v138, v1
	s_or_b64 exec, exec, s[6:7]
	s_and_saveexec_b64 s[6:7], s[4:5]
	s_cbranch_execz .LBB0_1758
	v_add_u32_e32 v1, s42, v173
	ds_write_b128 v1, v[130:133]

; #define LAS __attribute__((address_space(3)))
;     ...
; #pragma unroll
;         for (int g = 0; g < 8; ++g)
; #pragma unroll
;             for (int r = 0; r < 4; ++r) { mx[0] = fmaxf(mx[0], fabsf(v[g][r][0])); mx[1] = fmaxf(mx[1], fabsf(v[g][r][1])); mx[2] = fmaxf(mx[2], fabsf(v[g][r][2])); mx[3] = fmaxf(mx[3], fabsf(v[g][r][3])); }
; #pragma unroll
;         for (int c = 0; c < 4; ++c) { float m = mx[c]; m = fmaxf(m, __shfl_xor(m, 8)); m = fmaxf(m, __shfl_xor(m, 16)); m = fmaxf(m, __shfl_xor(m, 32)); mx[c] = m; }
;         if (tid == 0) MISC[2] = nxt;
;         if (kr == 0) *(LAS f32x4*)(smax + wave * 32 + 4 * n4) = mx;
.LBB0_1991:
	s_or_b64 exec, exec, s[6:7]
	s_waitcnt vmcnt(10)
	v_max3_f32 v130, |v2|, 0, |v6|
	s_waitcnt vmcnt(8)
	v_max3_f32 v130, v130, |v10|, |v14|
	s_waitcnt vmcnt(26)
	v_max3_f32 v130, v130, |v18|, |v22|
	s_waitcnt vmcnt(24)
	v_max3_f32 v130, v130, |v26|, |v30|
	s_waitcnt vmcnt(22)
	v_max3_f32 v130, v130, |v34|, |v38|
	s_waitcnt vmcnt(20)
	v_max3_f32 v130, v130, |v42|, |v46|
	v_max3_f32 v131, |v3|, 0, |v7|
	s_waitcnt vmcnt(18)
	v_max3_f32 v130, v130, |v50|, |v54|
	v_max3_f32 v132, |v4|, 0, |v8|
	v_max3_f32 v131, v131, |v11|, |v15|
	s_waitcnt vmcnt(16)
	v_max3_f32 v130, v130, |v58|, |v62|
	v_max3_f32 v132, v132, |v12|, |v16|
	v_max3_f32 v131, v131, |v19|, |v23|
	s_waitcnt vmcnt(14)
	v_max3_f32 v130, v130, |v66|, |v70|
	v_max3_f32 v132, v132, |v20|, |v24|
	v_max3_f32 v131, v131, |v27|, |v31|
	s_waitcnt vmcnt(12)
	v_max3_f32 v130, v130, |v74|, |v78|
	v_max3_f32 v132, v132, |v28|, |v32|
	v_max3_f32 v131, v131, |v35|, |v39|
	s_waitcnt vmcnt(10)
	v_max3_f32 v130, v130, |v82|, |v86|
	v_max3_f32 v132, v132, |v36|, |v40|
	v_max3_f32 v131, v131, |v43|, |v47|
	s_waitcnt vmcnt(8)
	v_max3_f32 v130, v130, |v90|, |v94|
	v_max3_f32 v132, v132, |v44|, |v48|
	v_max3_f32 v131, v131, |v51|, |v55|
	s_waitcnt vmcnt(6)
	v_max3_f32 v130, v130, |v98|, |v102|
	v_max3_f32 v133, |v5|, 0, |v9|
	v_max3_f32 v132, v132, |v52|, |v56|
	v_max3_f32 v131, v131, |v59|, |v63|
	s_waitcnt vmcnt(4)
	v_max3_f32 v130, v130, |v106|, |v110|
	v_max3_f32 v133, v133, |v13|, |v17|
	v_max3_f32 v132, v132, |v60|, |v64|
	v_max3_f32 v131, v131, |v67|, |v71|
	s_waitcnt vmcnt(2)
	v_max3_f32 v130, v130, |v114|, |v118|
	v_max3_f32 v133, v133, |v21|, |v25|
	v_max3_f32 v132, v132, |v68|, |v72|
	v_max3_f32 v131, v131, |v75|, |v79|
	s_waitcnt vmcnt(0)
	v_max3_f32 v130, v130, |v122|, |v126|
	v_max3_f32 v133, v133, |v29|, |v33|
	v_max3_f32 v132, v132, |v76|, |v80|
	v_max3_f32 v131, v131, |v83|, |v87|
	v_max3_f32 v133, v133, |v37|, |v41|
	v_max3_f32 v132, v132, |v84|, |v88|
	v_max3_f32 v131, v131, |v91|, |v95|
	v_max3_f32 v133, v133, |v45|, |v49|
	v_max3_f32 v132, v132, |v92|, |v96|
	v_max3_f32 v131, v131, |v99|, |v103|
	v_max3_f32 v133, v133, |v53|, |v57|
	v_max3_f32 v132, v132, |v100|, |v104|
	v_max3_f32 v131, v131, |v107|, |v111|
	v_max3_f32 v133, v133, |v61|, |v65|
	v_max3_f32 v132, v132, |v108|, |v112|
	v_max3_f32 v131, v131, |v115|, |v119|
	v_max3_f32 v133, v133, |v69|, |v73|
	v_max3_f32 v132, v132, |v116|, |v120|
	v_max3_f32 v131, v131, |v123|, |v127|
	v_max3_f32 v133, v133, |v77|, |v81|
	v_max3_f32 v135, v132, |v124|, |v128|
	v_max3_f32 v133, v133, |v85|, |v89|
	v_max3_f32 v133, v133, |v93|, |v97|
	v_max3_f32 v133, v133, |v101|, |v105|
	v_max3_f32 v133, v133, |v109|, |v113|
	v_max3_f32 v133, v133, |v117|, |v121|
	v_max3_f32 v133, v133, |v125|, |v129|
	v_mov_b32_e32 v132, v135
	s_nop 1
	v_max_f32_dpp v130, v130, v130 row_ror:8 row_mask:0xf bank_mask:0xf
	v_max_f32_dpp v131, v131, v131 row_ror:8 row_mask:0xf bank_mask:0xf
	v_max_f32_dpp v132, v132, v132 row_ror:8 row_mask:0xf bank_mask:0xf
	v_max_f32_dpp v133, v133, v133 row_ror:8 row_mask:0xf bank_mask:0xf
	v_mov_b32_e32 v134, v130
	v_mov_b32_e32 v136, v131
	v_mov_b32_e32 v137, v132
	v_mov_b32_e32 v138, v133
	s_nop 1
	v_permlane16_swap_b32 v130, v134
	v_permlane16_swap_b32 v131, v136
	v_permlane16_swap_b32 v132, v137
	v_permlane16_swap_b32 v133, v138
	v_max_f32_e32 v130, v130, v134
	v_max_f32_e32 v131, v131, v136
	v_max_f32_e32 v132, v132, v137
	v_max_f32_e32 v133, v133, v138
	v_mov_b32_e32 v134, v130
	v_mov_b32_e32 v136, v131
	v_mov_b32_e32 v137, v132
	v_mov_b32_e32 v138, v133
	s_nop 1
	v_permlane32_swap_b32 v130, v134
	v_permlane32_swap_b32 v131, v136
	v_permlane32_swap_b32 v132, v137
	v_permlane32_swap_b32 v133, v138
	v_max_f32_e32 v130, v130, v134
	v_max_f32_e32 v131, v131, v136
	v_max_f32_e32 v132, v132, v137
	v_max_f32_e32 v133, v133, v138
	s_and_saveexec_b64 s[6:7], s[40:41]
	v_mov_b32_e32 v138, s69
	ds_write_b32 v138, v1
	s_or_b64 exec, exec, s[6:7]
	s_and_saveexec_b64 s[6:7], s[4:5]
	s_cbranch_execz .LBB0_1995
	v_add_u32_e32 v1, s38, v169
	ds_write_b128 v1, v[130:133]
